# phase 5: workgroups with bid bit 3 set run the HBM-bound lru_pass2 before their attention unit, the others after (halves the number of workgroups competing for HBM at a time)
# speedup vs baseline: 1.0190x; 1.0112x over previous
; #define LAS __attribute__((address_space(3)))
; template <int DQ>
; DI AtDma at_dma_init(int ld_bytes, int wave, int lane) {
;     AtDma d; d.rope = 0u;
;     constexpr int PPR = DQ / 8;
; #pragma unroll
;     for (int k = 0; k < DQ / 64; ++k) { const int L = (wave + 8 * k) * 64 + lane, r = L / PPR, pc = (L % PPR) ^ at_kf<DQ>(r);
;         if (DQ == 192 && pc >= 16) { d.ko[k] = (unsigned)(r * 128 + (pc - 16) * 16); d.rope |= 1u << k; } else d.ko[k] = (unsigned)(r * ld_bytes + pc * 16); }
;     if (DQ == 128) d.ko[2] = 0u;
; #pragma unroll
;     for (int k = 0; k < 2; ++k) { const int L = (wave + 8 * k) * 64 + lane, r = L >> 4, pc = (L & 15) ^ (2 * (r & 7)); d.vo[k] = (unsigned)(r * ld_bytes + pc * 16); }
;     return d;
; DI void phase_attn0(const Params& p, LAS unsigned char* lds, int G, int bid) {
;     const int tid = threadIdx.x, lane = tid & 63, wave = __builtin_amdgcn_readfirstlane(tid >> 6), h = lane >> 5;
;     const bf16_t* Q0 = (const bf16_t*)(p.ws + WS_Q0);
;     bf16_t* Y = (bf16_t*)(p.ws + WS_Y);
;     const float c2 = 0.07216878364870322f * LOG2E;
;     const AtRd rd = at_rd_init<192>(lane);
;     const AtDma dm = at_dma_init<192>(4096, wave, lane);
;     for (int it = 0; it < 2; ++it)
;     for (int u = it == 0 ? bid : 256 + (bid + G - G / 2) % G; u < (it == 0 ? 256 : 256 + 32); u += G) {
;         MlaDrv T; T.KV = (const char*)(p.ws + WS_KV0); T.KR = (const char*)(p.ws + WS_KR);
;         int qrow, nt;
;         if (u < 256) { T.b = u >> 6; T.head = (u >> 3) & 7; nt = 36; qrow = NCTX + T.b * SEQ + (u & 7) * 256 + wave * 32 + (lane & 31); }
;         else { const int v = u - 256; T.b = v >> 3; T.head = v & 7; nt = 4; qrow = T.b * CTX + wave * 32 + (lane & 31); }
;         bf16x8 qf[12];
; #pragma unroll
;         for (int s = 0; s < 12; ++s) qf[s] = *(const bf16x8*)(Q0 + (size_t)qrow * 1536 + T.head * 192 + 16 * s + 8 * h);
.LBB0_530:
	s_cmp_gt_i32 s24, 5
	s_cselect_b64 s[0:1], -1, 0
	s_cmp_lt_i32 s25, 6
	s_cselect_b64 s[2:3], -1, 0
	s_or_b64 s[0:1], s[0:1], s[2:3]
	s_and_b64 vcc, exec, s[0:1]
	s_cbranch_vccnz .LBB0_622
	s_mov_b32 s97, 0
	s_and_b32 s0, s26, 6
	s_cmp_lg_u32 s0, 0
	s_cbranch_scc1 .Lp5_normal
	s_bitcmp1_b32 s22, 3
	s_cbranch_scc0 .Lp5_normal
	s_mov_b32 s97, 1
	s_branch .LBB0_560
.Lp5_normal:
	s_bitcmp1_b32 s26, 1
	s_cbranch_scc1 .LBB0_560
.Lp5_mla:
	v_readfirstlane_b32 s2, v0
	s_movk_i32 s0, 0xffc0
	s_nop 0
	v_mov_b32_e32 v1, s2
	v_bfi_b32 v2, s0, v1, v0
	s_mov_b32 s0, 0x2aaaaaab
	v_mul_hi_i32 v1, v2, s0
	v_lshrrev_b32_e32 v3, 31, v1
	v_ashrrev_i32_e32 v1, 2, v1
	v_add_u32_e32 v1, v1, v3
	v_mul_lo_u32 v3, v1, 24
	v_sub_u32_e32 v3, v2, v3
	v_lshrrev_b32_e32 v4, 1, v1
	v_bitop3_b32 v3, v4, v3, 7 bitop3:0x6c
	v_cmp_gt_i32_e32 vcc, 16, v3
	v_lshlrev_b32_e32 v3, 4, v3
	s_and_saveexec_b64 s[0:1], vcc
	s_xor_b64 s[0:1], exec, s[0:1]
	v_lshl_add_u32 v162, v1, 12, v3
	s_or_saveexec_b64 s[0:1], s[0:1]
	v_mov_b32_e32 v4, 0
	s_xor_b64 exec, exec, s[0:1]
	v_lshlrev_b32_e32 v1, 7, v1
	s_movk_i32 s3, 0xff00
	v_add3_u32 v162, v1, v3, s3
	v_mov_b32_e32 v4, 1
	s_or_b64 exec, exec, s[0:1]
	v_add_u32_e32 v5, 0x200, v2
	s_mov_b32 s0, 0x2aaaaaab
	v_mul_hi_i32 v1, v5, s0
	v_lshrrev_b32_e32 v3, 31, v1
	v_ashrrev_i32_e32 v1, 2, v1
	v_add_u32_e32 v1, v1, v3
	v_mul_lo_u32 v3, v1, 24
	v_sub_u32_e32 v3, v5, v3
	v_lshrrev_b32_e32 v6, 1, v1
	v_bitop3_b32 v3, v6, v3, 7 bitop3:0x6c
	v_cmp_gt_i32_e32 vcc, 16, v3
	v_lshlrev_b32_e32 v3, 4, v3
	s_and_saveexec_b64 s[0:1], vcc
	s_xor_b64 s[0:1], exec, s[0:1]
	v_lshl_add_u32 v164, v1, 12, v3
	s_andn2_saveexec_b64 s[0:1], s[0:1]
	v_lshlrev_b32_e32 v1, 7, v1
	s_movk_i32 s3, 0xff00
	v_add3_u32 v164, v1, v3, s3
	v_or_b32_e32 v4, 2, v4
	s_or_b64 exec, exec, s[0:1]
	v_add_u32_e32 v3, 0x400, v2
	s_mov_b32 s0, 0x2aaaaaab
	v_mul_hi_i32 v1, v3, s0
	v_lshrrev_b32_e32 v6, 31, v1
	v_ashrrev_i32_e32 v1, 2, v1
	v_add_u32_e32 v1, v1, v6
	v_mul_lo_u32 v6, v1, 24
	v_sub_u32_e32 v3, v3, v6
	v_lshrrev_b32_e32 v6, 1, v1
	v_bitop3_b32 v3, v6, v3, 7 bitop3:0x6c
	v_cmp_gt_i32_e32 vcc, 16, v3
	v_lshlrev_b32_e32 v6, 4, v3
	s_and_saveexec_b64 s[0:1], vcc
	s_xor_b64 s[0:1], exec, s[0:1]
	v_lshl_add_u32 v166, v1, 12, v6
	s_or_saveexec_b64 s[0:1], s[0:1]
	v_and_b32_e32 v3, 63, v0
	s_xor_b64 exec, exec, s[0:1]
	v_lshlrev_b32_e32 v1, 7, v1
	s_movk_i32 s3, 0xff00
	v_add3_u32 v166, v1, v6, s3
	v_or_b32_e32 v4, 4, v4
	s_or_b64 exec, exec, s[0:1]
	v_lshrrev_b32_e32 v6, 5, v3
	v_bfe_u32 v10, v0, 1, 3
	s_lshr_b32 s2, s2, 6
	v_bitop3_b32 v11, v6, v10, 2 bitop3:0x36
	s_add_u32 s0, s50, 0x2c5ae000
	v_lshrrev_b32_e32 v1, 1, v0
	v_lshlrev_b32_e32 v180, 4, v11
	v_bitop3_b32 v11, v6, v10, 4 bitop3:0x36
	v_bitop3_b32 v10, v6, v10, 6 bitop3:0x36
	s_addc_u32 s1, s51, 0
	v_bitop3_b32 v1, v6, v1, 7 bitop3:0x78
	v_lshlrev_b32_e32 v182, 4, v10
	v_bfe_u32 v10, v3, 2, 2
	v_lshlrev_b32_e32 v6, 2, v6
	s_add_u32 s8, s50, 0x304ae000
	v_lshrrev_b32_e32 v8, 2, v3
	v_lshrrev_b32_e32 v9, 4, v3
	v_lshlrev_b32_e32 v181, 4, v11
	v_bfe_u32 v3, v3, 4, 1
	v_or_b32_e32 v11, v6, v10
	s_addc_u32 s9, s51, 0
	v_bitop3_b32 v14, v6, v3, v10 bitop3:0x36
	v_bitop3_b32 v3, v3, v11, 4 bitop3:0x36
	s_lshr_b32 s4, s23, 31
	v_and_b32_e32 v7, 31, v0
	v_lshlrev_b32_e32 v183, 5, v14
	v_or_b32_e32 v14, 2, v9
	v_lshlrev_b32_e32 v185, 5, v3
	v_or_b32_e32 v3, 6, v9
	s_movk_i32 s3, 0x180
	s_add_i32 s4, s23, s4
	v_ashrrev_i32_e32 v2, 4, v2
	v_bitop3_b32 v14, v6, v14, v10 bitop3:0x36
	v_bitop3_b32 v3, v6, v3, v10 bitop3:0x36
	v_and_b32_e32 v9, 15, v0
	v_mad_u32_u24 v187, v7, s3, 0
	s_add_i32 s3, s23, s22
	s_ashr_i32 s4, s4, 1
	v_lshlrev_b32_e32 v10, 1, v2
	s_sub_i32 s10, s3, s4
	v_bitop3_b32 v10, v10, v9, 14 bitop3:0x6c
	v_lshlrev_b32_e32 v2, 12, v2
	s_add_u32 s12, s50, 0x2e0ae000
	v_lshl_or_b32 v168, v10, 4, v2
	v_ashrrev_i32_e32 v2, 4, v5
	s_addc_u32 s13, s51, 0
	v_lshlrev_b32_e32 v5, 1, v2
	s_add_u32 s14, s50, 0x2c48e000
	v_bitop3_b32 v5, v5, v9, 14 bitop3:0x6c
	v_lshlrev_b32_e32 v2, 12, v2
	s_addc_u32 s15, s51, 0
	v_lshl_or_b32 v170, v5, 4, v2
	v_lshl_or_b32 v189, s2, 5, v7
	s_lshl_b32 s2, s2, 10
	v_and_b32_e32 v2, 1, v4
	s_add_i32 s27, s2, 0
	v_cmp_eq_u32_e64 s[2:3], 0, v2
	v_and_b32_e32 v2, 2, v4
	s_abs_i32 s16, s23
	v_cmp_eq_u32_e64 s[4:5], 0, v2
	v_cvt_f32_u32_e32 v2, s16
	s_sub_i32 s18, 0, s16
	s_ashr_i32 s17, s10, 31
	s_abs_i32 s10, s10
	v_rcp_iflag_f32_e32 v2, v2
	v_lshlrev_b32_e32 v13, 3, v0
	v_lshlrev_b32_e32 v186, 5, v3
	v_lshrrev_b32_e32 v3, 2, v0
	v_mul_f32_e32 v2, 0x4f7ffffe, v2
	v_cvt_u32_f32_e32 v2, v2
	v_lshlrev_b32_e32 v12, 8, v11
	v_and_b32_e32 v13, 24, v13
	v_and_b32_e32 v6, 8, v3
	v_readfirstlane_b32 s19, v2
	s_mul_i32 s18, s18, s19
	s_mul_hi_u32 s18, s19, s18
	s_add_i32 s19, s19, s18
	s_mul_hi_u32 s18, s10, s19
	s_mul_i32 s18, s18, s16
	s_sub_i32 s10, s10, s18
	s_sub_i32 s18, s10, s16
	s_cmp_ge_u32 s10, s16
	s_cselect_b32 s10, s18, s10
	s_sub_i32 s18, s10, s16
	s_cmp_ge_u32 s10, s16
	s_cselect_b32 s10, s18, s10
	s_xor_b32 s10, s10, s17
	v_mov_b32_e32 v3, 0
	v_and_b32_e32 v8, 8, v8
	v_and_b32_e32 v4, 4, v4
	s_sub_i32 s34, s10, s17
	v_mbcnt_lo_u32_b32 v2, -1, 0
	v_lshlrev_b32_e32 v1, 4, v1
	v_lshlrev_b32_e32 v184, 5, v14
	s_mov_b32 s11, 0
	v_add3_u32 v188, 0, v12, v13
	v_add_u32_e32 v190, 0x400, v189
	v_mov_b32_e32 v163, v3
	v_mov_b32_e32 v165, v3
	v_cmp_eq_u32_e64 s[6:7], 0, v4
	v_mov_b32_e32 v167, v3
	v_mov_b32_e32 v169, v3
	v_mov_b32_e32 v171, v3
	s_addk_i32 s34, 0x100
	s_mov_b64 s[16:17], -1
	s_movk_i32 s35, 0xc00
	v_lshlrev_b32_e32 v172, 1, v6
	s_add_i32 s40, s27, 0x2000
	s_add_i32 s41, s27, 0x4000
	s_mov_b64 s[18:19], 0x100
	s_add_i32 s54, s27, 0x12000
	s_add_i32 s55, s27, 0x14000
	s_mov_b32 s58, 0x41000000
	v_lshlrev_b32_e32 v174, 1, v8
	v_mbcnt_hi_u32_b32 v191, -1, v2
	v_mov_b32_e32 v248, 0x2000
	v_mov_b32_e32 v249, 0x40000
	v_cndmask_b32_e64 v234, v248, v249, s[2:3]
	v_mov_b32_e32 v235, 0
	v_cndmask_b32_e64 v236, v248, v249, s[4:5]
	v_mov_b32_e32 v237, 0
	v_cndmask_b32_e64 v238, v248, v249, s[6:7]
	v_mov_b32_e32 v239, 0
	s_mov_b32 s84, 0x40000
	s_mov_b32 s85, 0
	v_add_u32_e32 v240, v187, v1
	v_add_u32_e32 v241, v187, v180
	v_add_u32_e32 v242, v187, v181
	v_add_u32_e32 v243, v187, v182
	v_add_u32_e32 v244, 0x12000, v188
	v_add_u32_e32 v245, v244, v184
	v_add_u32_e32 v246, v244, v185
	v_add_u32_e32 v247, v244, v186
	v_add_u32_e32 v244, v244, v183
	s_branch .LBB0_546

; #define LAS __attribute__((address_space(3)))
; #define SEAM(k) do { if (rep_ == REP(k) && IN((k) + 1)) xcd_barrier(bar); } while (0)
; DI void lru_pass2(const Params& p, LAS unsigned char* lds, int G, int bid) {
;     const int tid = threadIdx.x;
;     const bf16_t* Z = (const bf16_t*)(p.ws + WS_Z);
;     const unsigned* ABG = (const unsigned*)(p.ws + WS_ABG); const float* CARRY = (const float*)(p.ws + WS_CARRY);
;     bf16_t* Y = (bf16_t*)(p.ws + WS_Y);
;     LAS float* HB = (LAS float*)lds;
;     const int NU = NCHUNK * NB * 8;
;     const bool special = (G == 256);
;     const bool ctxwg = special && bid >= 128 && bid < 160;
;     const int ustart = !special ? bid : (ctxwg ? (NU - 32) + (bid - 128) : (bid < 128 ? bid : bid - 32));
;     const int ustep = !special ? G : (ctxwg ? NU : 224), uend = !special ? NU : (ctxwg ? NU : NU - 32);
;     for (int u = ustart; u < uend; u += ustep) {
;         const int n = u & 7, bc = u >> 3, b = bc & 3, ci = bc >> 2;
;         const int t0 = ci < 4 ? 64 * ci : 64 * (ci - 4);
;         const int row0 = ci < 4 ? b * CTX + t0 : NCTX + b * SEQ + t0;
;         const int c4 = (tid & 31) * 4, tb = 4 * (tid >> 5), cg = 128 * n + c4;
;         u32x2 grw[4];
; #pragma unroll
;         for (int j = 0; j < 4; ++j) grw[j] = *(const u32x2*)(Z + (size_t)(row0 + tb + j) * L0INP + 1856 + cg);
; __global__ void __launch_bounds__(NTHREADS, 2) fwd_kernel(Params p) {
;     ...
;     if (IN(5)) for (int rep_ = 0; rep_ <= REP(5); ++rep_) { if (rep_) __syncthreads(); if (!(p.flags & 2)) phase_attn0(p, lds, G, bid); __syncthreads(); if (!(p.flags & 4)) lru_pass2(p, lds, G, bid); SEAM(5); }
.LBB0_560:
	s_bitcmp1_b32 s26, 2
	s_waitcnt vmcnt(0)
	s_barrier
	s_cbranch_scc1 .LBB0_572
	s_cmp_eq_u32 s97, 2
	s_cbranch_scc1 .LBB0_572
	s_cmpk_eq_i32 s23, 0x100
	s_cselect_b64 s[0:1], -1, 0
	s_cmpk_gt_i32 s22, 0x7f
	s_cselect_b64 s[2:3], -1, 0
	s_and_b64 s[0:1], s[2:3], s[0:1]
	s_cmpk_lt_u32 s22, 0xa0
	s_cselect_b64 s[2:3], -1, 0
	s_and_b64 s[2:3], s[0:1], s[2:3]
	s_sub_i32 s0, s22, 32
	s_cmpk_lt_i32 s22, 0x80
	s_cselect_b32 s4, s22, s0
	s_add_i32 s5, s22, 0x3e0
	s_and_b64 s[0:1], s[2:3], exec
	s_cselect_b32 s4, s5, s4
	s_cmpk_eq_i32 s23, 0x100
	s_cselect_b64 s[0:1], -1, 0
	s_and_b64 s[0:1], s[0:1], exec
	s_cselect_b32 s14, s4, s22
	s_movk_i32 s4, 0x480
	s_and_b64 s[0:1], s[2:3], exec
	s_cselect_b32 s6, s4, 0x460
	s_cmpk_eq_i32 s23, 0x100
	s_cselect_b64 s[4:5], -1, 0
	s_and_b64 s[0:1], s[4:5], exec
	s_cselect_b32 s15, s6, 0x480
	s_cmp_ge_i32 s14, s15
	s_movk_i32 s6, 0x7f
	s_cbranch_scc1 .LBB0_572
	v_lshlrev_b32_e32 v5, 2, v0
	v_lshrrev_b32_e32 v10, 3, v0
	v_and_b32_e32 v12, 0x7f, v0
	s_add_u32 s0, s50, 0x32aee000
	v_and_b32_e32 v2, 0x7c, v5
	v_and_b32_e32 v1, 60, v10
	v_mov_b32_e32 v7, 0
	v_lshlrev_b32_e32 v6, 2, v12
	s_addc_u32 s1, s51, 0
	v_lshl_add_u64 v[8:9], s[50:51], 0, v[6:7]
	v_add_u32_e32 v26, 0, v6
	v_lshlrev_b32_e32 v6, 9, v1
	v_lshlrev_b32_e32 v11, 2, v2
	v_or_b32_e32 v28, 1, v1
	s_movk_i32 s7, 0xe0
	s_and_b64 s[2:3], s[2:3], exec
	v_add3_u32 v27, 0, v6, v11
	v_lshlrev_b32_e32 v6, 9, v28
	v_or_b32_e32 v30, 2, v1
	s_cselect_b32 s7, 0x480, s7
	s_and_b64 s[2:3], s[4:5], exec
	v_add3_u32 v29, 0, v6, v11
	v_lshlrev_b32_e32 v6, 9, v30
	v_or_b32_e32 v32, 3, v10
	s_movk_i32 s2, 0xff
	v_lshrrev_b32_e32 v4, 7, v0
	s_mov_b64 s[4:5], 0x3d376000
	v_add3_u32 v31, 0, v6, v11
	v_lshlrev_b32_e32 v6, 9, v32
	s_cselect_b32 s16, s7, s23
	v_cmp_lt_u32_e64 s[2:3], s2, v0
	v_lshl_add_u64 v[8:9], v[8:9], 0, s[4:5]
	v_lshlrev_b32_e32 v3, 2, v4
	v_cmp_lt_u32_e64 s[4:5], s6, v0
	s_mov_b32 s7, 0
	v_add_u32_e32 v5, 0, v5
	v_add3_u32 v33, 0, v6, v11
	s_movk_i32 s17, 0x1800
	v_mov_b64_e32 v[10:11], s[50:51]
	s_mov_b32 s18, 0x2660e000
	s_movk_i32 s19, 0x1000
	s_movk_i32 s27, 0x2000
	s_movk_i32 s30, 0x3000
	s_movk_i32 s31, 0x4000
	s_movk_i32 s34, 0x5000
	s_movk_i32 s35, 0x6000
	s_movk_i32 s40, 0x7000
	v_lshlrev_b32_e32 v12, 2, v12
	s_mov_b32 s41, 0x304ae000
	s_branch .LBB0_565

; #define SEAM(k) do { if (rep_ == REP(k) && IN((k) + 1)) xcd_barrier(bar); } while (0)
; __global__ void __launch_bounds__(NTHREADS, 2) fwd_kernel(Params p) {
;     ...
;     if (IN(5)) for (int rep_ = 0; rep_ <= REP(5); ++rep_) { if (rep_) __syncthreads(); if (!(p.flags & 2)) phase_attn0(p, lds, G, bid); __syncthreads(); if (!(p.flags & 4)) lru_pass2(p, lds, G, bid); SEAM(5); }
.LBB0_572:
	s_cmp_eq_u32 s97, 1
	s_cbranch_scc0 .Lp5_end
	s_mov_b32 s97, 2
	s_branch .Lp5_mla
